# P4 job prologue: raw-gate staging keeps its 8 loads in flight (counted waits) instead of 4 serialized load/wait/ds_write pairs
# speedup vs baseline: 1.0154x; 1.0048x over previous
.LBB0_623:
	v_and_b32_e32 v11, 0x7fffff80, v6
	v_and_b32_e32 v10, 0x7fffff80, v7
	v_add_u32_e32 v11, v11, v132
	v_add_u32_e32 v10, v10, v1
	v_sub_u32_e32 v12, 0x7ff, v11
	v_sub_u32_e32 v13, 0x7ff, v10
	v_cndmask_b32_e32 v11, v12, v11, vcc
	v_sub_u32_e32 v12, 0xff, v6
	v_cndmask_b32_e32 v10, v13, v10, vcc
	v_sub_u32_e32 v13, 0xff, v7
	v_cndmask_b32_e32 v12, v12, v6, vcc
	v_cmp_gt_i32_e64 s[0:1], s49, v6
	v_add_u32_e32 v11, s47, v11
	v_cndmask_b32_e32 v13, v13, v7, vcc
	v_add_u32_e32 v12, s34, v12
	v_cmp_gt_i32_e64 s[2:3], s49, v7
	v_add_u32_e32 v10, s47, v10
	v_add_u32_e32 v13, s34, v13
	v_cndmask_b32_e64 v12, v11, v12, s[0:1]
	v_cndmask_b32_e64 v10, v10, v13, s[2:3]
	v_ashrrev_i32_e32 v13, 31, v12
	v_ashrrev_i32_e32 v11, 31, v10
	v_lshlrev_b64 v[12:13], 6, v[12:13]
	v_lshlrev_b64 v[10:11], 6, v[10:11]
	v_lshl_add_u64 v[12:13], s[36:37], 0, v[12:13]
	v_lshl_add_u64 v[10:11], s[36:37], 0, v[10:11]
	global_load_dword v202, v[12:13], off
	global_load_dword v203, v[10:11], off
	v_add_u32_e32 v8, -2, v8
	s_add_i32 s48, s48, 4
	global_load_dword v204, v[12:13], off offset:16
	s_nop 0
	global_load_dword v205, v[10:11], off offset:16
	v_add_u32_e32 v11, 0x400, v6
	v_and_b32_e32 v13, 0x7fffff80, v11
	v_add_u32_e32 v13, v13, v132
	v_sub_u32_e32 v14, 0x7ff, v13
	v_cndmask_b32_e32 v13, v14, v13, vcc
	v_sub_u32_e32 v14, 0xfffffcff, v6
	v_cmp_gt_i32_e64 s[0:1], s49, v11
	v_cndmask_b32_e32 v11, v14, v11, vcc
	v_add_u32_e32 v13, s47, v13
	v_add_u32_e32 v11, s34, v11
	v_add_u32_e32 v6, 0x800, v6
	v_add_u32_e32 v10, 0x400, v7
	v_and_b32_e32 v12, 0x7fffff80, v10
	v_add_u32_e32 v12, v12, v1
	v_sub_u32_e32 v15, 0x7ff, v12
	v_cndmask_b32_e32 v12, v15, v12, vcc
	v_sub_u32_e32 v15, 0xfffffcff, v7
	v_cmp_gt_i32_e64 s[2:3], s49, v10
	v_cndmask_b32_e32 v10, v15, v10, vcc
	v_add_u32_e32 v12, s47, v12
	v_add_u32_e32 v10, s34, v10
	v_cndmask_b32_e64 v10, v12, v10, s[2:3]
	v_cndmask_b32_e64 v12, v13, v11, s[0:1]
	v_ashrrev_i32_e32 v13, 31, v12
	v_ashrrev_i32_e32 v11, 31, v10
	v_lshlrev_b64 v[12:13], 6, v[12:13]
	v_lshlrev_b64 v[10:11], 6, v[10:11]
	v_lshl_add_u64 v[12:13], s[36:37], 0, v[12:13]
	v_lshl_add_u64 v[10:11], s[36:37], 0, v[10:11]
	global_load_dword v206, v[12:13], off
	global_load_dword v207, v[10:11], off
	v_cmp_eq_u32_e64 s[0:1], 0, v8
	v_add_u32_e32 v7, 0x800, v7
	s_or_b64 s[86:87], s[0:1], s[86:87]
	global_load_dword v208, v[12:13], off offset:16
	s_nop 0
	global_load_dword v209, v[10:11], off offset:16
	s_waitcnt vmcnt(6)
	ds_write2st64_b32 v9, v202, v203 offset1:8
	s_waitcnt vmcnt(4)
	ds_write2st64_b32 v9, v204, v205 offset0:36 offset1:44
	s_waitcnt vmcnt(2)
	ds_write2st64_b32 v9, v206, v207 offset0:16 offset1:24
	s_waitcnt vmcnt(0)
	ds_write2st64_b32 v9, v208, v209 offset0:52 offset1:60
	v_add_u32_e32 v9, 0x2000, v9
	v_mov_b32_e32 v10, s48
	s_andn2_b64 exec, exec, s[86:87]
	s_cbranch_execnz .LBB0_623
	s_or_b64 exec, exec, s[86:87]
	v_lshlrev_b32_e32 v8, 9, v10

.LBB0_2023:
	v_and_b32_e32 v11, 0x7fffff80, v6
	v_and_b32_e32 v10, 0x7fffff80, v7
	v_add_u32_e32 v11, v11, v128
	v_add_u32_e32 v10, v10, v1
	v_sub_u32_e32 v12, 0x7ff, v11
	v_sub_u32_e32 v13, 0x7ff, v10
	v_cndmask_b32_e32 v11, v12, v11, vcc
	v_sub_u32_e32 v12, 0xff, v6
	v_cndmask_b32_e32 v10, v13, v10, vcc
	v_sub_u32_e32 v13, 0xff, v7
	v_cndmask_b32_e32 v12, v12, v6, vcc
	v_cmp_gt_i32_e64 s[0:1], s52, v6
	v_add_u32_e32 v11, s41, v11
	v_cndmask_b32_e32 v13, v13, v7, vcc
	v_add_u32_e32 v12, s30, v12
	v_cmp_gt_i32_e64 s[2:3], s52, v7
	v_add_u32_e32 v10, s41, v10
	v_add_u32_e32 v13, s30, v13
	v_cndmask_b32_e64 v12, v11, v12, s[0:1]
	v_cndmask_b32_e64 v10, v10, v13, s[2:3]
	v_ashrrev_i32_e32 v13, 31, v12
	v_ashrrev_i32_e32 v11, 31, v10
	v_lshlrev_b64 v[12:13], 6, v[12:13]
	v_lshlrev_b64 v[10:11], 6, v[10:11]
	v_lshl_add_u64 v[12:13], s[34:35], 0, v[12:13]
	v_lshl_add_u64 v[10:11], s[34:35], 0, v[10:11]
	global_load_dword v202, v[12:13], off
	global_load_dword v203, v[10:11], off
	v_add_u32_e32 v8, -2, v8
	s_add_i32 s51, s51, 4
	global_load_dword v204, v[12:13], off offset:16
	s_nop 0
	global_load_dword v205, v[10:11], off offset:16
	v_add_u32_e32 v11, 0x400, v6
	v_and_b32_e32 v13, 0x7fffff80, v11
	v_add_u32_e32 v13, v13, v128
	v_sub_u32_e32 v14, 0x7ff, v13
	v_cndmask_b32_e32 v13, v14, v13, vcc
	v_sub_u32_e32 v14, 0xfffffcff, v6
	v_cmp_gt_i32_e64 s[0:1], s52, v11
	v_cndmask_b32_e32 v11, v14, v11, vcc
	v_add_u32_e32 v13, s41, v13
	v_add_u32_e32 v11, s30, v11
	v_add_u32_e32 v6, 0x800, v6
	v_add_u32_e32 v10, 0x400, v7
	v_and_b32_e32 v12, 0x7fffff80, v10
	v_add_u32_e32 v12, v12, v1
	v_sub_u32_e32 v15, 0x7ff, v12
	v_cndmask_b32_e32 v12, v15, v12, vcc
	v_sub_u32_e32 v15, 0xfffffcff, v7
	v_cmp_gt_i32_e64 s[2:3], s52, v10
	v_cndmask_b32_e32 v10, v15, v10, vcc
	v_add_u32_e32 v12, s41, v12
	v_add_u32_e32 v10, s30, v10
	v_cndmask_b32_e64 v10, v12, v10, s[2:3]
	v_cndmask_b32_e64 v12, v13, v11, s[0:1]
	v_ashrrev_i32_e32 v13, 31, v12
	v_ashrrev_i32_e32 v11, 31, v10
	v_lshlrev_b64 v[12:13], 6, v[12:13]
	v_lshlrev_b64 v[10:11], 6, v[10:11]
	v_lshl_add_u64 v[12:13], s[34:35], 0, v[12:13]
	v_lshl_add_u64 v[10:11], s[34:35], 0, v[10:11]
	global_load_dword v206, v[12:13], off
	global_load_dword v207, v[10:11], off
	v_cmp_eq_u32_e64 s[0:1], 0, v8
	v_add_u32_e32 v7, 0x800, v7
	s_or_b64 s[86:87], s[0:1], s[86:87]
	global_load_dword v208, v[12:13], off offset:16
	s_nop 0
	global_load_dword v209, v[10:11], off offset:16
	s_waitcnt vmcnt(6)
	ds_write2st64_b32 v9, v202, v203 offset1:8
	s_waitcnt vmcnt(4)
	ds_write2st64_b32 v9, v204, v205 offset0:36 offset1:44
	s_waitcnt vmcnt(2)
	ds_write2st64_b32 v9, v206, v207 offset0:16 offset1:24
	s_waitcnt vmcnt(0)
	ds_write2st64_b32 v9, v208, v209 offset0:52 offset1:60
	v_add_u32_e32 v9, 0x2000, v9
	v_mov_b32_e32 v10, s51
	s_andn2_b64 exec, exec, s[86:87]
	s_cbranch_execnz .LBB0_2023
	s_or_b64 exec, exec, s[86:87]
	v_lshlrev_b32_e32 v8, 9, v10

.LBB0_3640:
	v_and_b32_e32 v11, 0x7fffff80, v6
	v_and_b32_e32 v10, 0x7fffff80, v7
	v_add_u32_e32 v11, v11, v128
	v_add_u32_e32 v10, v10, v1
	v_sub_u32_e32 v12, 0x7ff, v11
	v_sub_u32_e32 v13, 0x7ff, v10
	v_cndmask_b32_e32 v11, v12, v11, vcc
	v_sub_u32_e32 v12, 0xff, v6
	v_cndmask_b32_e32 v10, v13, v10, vcc
	v_sub_u32_e32 v13, 0xff, v7
	v_cndmask_b32_e32 v12, v12, v6, vcc
	v_cmp_gt_i32_e64 s[0:1], s49, v6
	v_add_u32_e32 v11, s41, v11
	v_cndmask_b32_e32 v13, v13, v7, vcc
	v_add_u32_e32 v12, s34, v12
	v_cmp_gt_i32_e64 s[2:3], s49, v7
	v_add_u32_e32 v10, s41, v10
	v_add_u32_e32 v13, s34, v13
	v_cndmask_b32_e64 v12, v11, v12, s[0:1]
	v_cndmask_b32_e64 v10, v10, v13, s[2:3]
	v_ashrrev_i32_e32 v13, 31, v12
	v_ashrrev_i32_e32 v11, 31, v10
	v_lshlrev_b64 v[12:13], 6, v[12:13]
	v_lshlrev_b64 v[10:11], 6, v[10:11]
	v_lshl_add_u64 v[12:13], s[36:37], 0, v[12:13]
	v_lshl_add_u64 v[10:11], s[36:37], 0, v[10:11]
	global_load_dword v202, v[12:13], off
	global_load_dword v203, v[10:11], off
	v_add_u32_e32 v8, -2, v8
	s_add_i32 s48, s48, 4
	global_load_dword v204, v[12:13], off offset:16
	s_nop 0
	global_load_dword v205, v[10:11], off offset:16
	v_add_u32_e32 v11, 0x400, v6
	v_and_b32_e32 v13, 0x7fffff80, v11
	v_add_u32_e32 v13, v13, v128
	v_sub_u32_e32 v14, 0x7ff, v13
	v_cndmask_b32_e32 v13, v14, v13, vcc
	v_sub_u32_e32 v14, 0xfffffcff, v6
	v_cmp_gt_i32_e64 s[0:1], s49, v11
	v_cndmask_b32_e32 v11, v14, v11, vcc
	v_add_u32_e32 v13, s41, v13
	v_add_u32_e32 v11, s34, v11
	v_add_u32_e32 v6, 0x800, v6
	v_add_u32_e32 v10, 0x400, v7
	v_and_b32_e32 v12, 0x7fffff80, v10
	v_add_u32_e32 v12, v12, v1
	v_sub_u32_e32 v15, 0x7ff, v12
	v_cndmask_b32_e32 v12, v15, v12, vcc
	v_sub_u32_e32 v15, 0xfffffcff, v7
	v_cmp_gt_i32_e64 s[2:3], s49, v10
	v_cndmask_b32_e32 v10, v15, v10, vcc
	v_add_u32_e32 v12, s41, v12
	v_add_u32_e32 v10, s34, v10
	v_cndmask_b32_e64 v10, v12, v10, s[2:3]
	v_cndmask_b32_e64 v12, v13, v11, s[0:1]
	v_ashrrev_i32_e32 v13, 31, v12
	v_ashrrev_i32_e32 v11, 31, v10
	v_lshlrev_b64 v[12:13], 6, v[12:13]
	v_lshlrev_b64 v[10:11], 6, v[10:11]
	v_lshl_add_u64 v[12:13], s[36:37], 0, v[12:13]
	v_lshl_add_u64 v[10:11], s[36:37], 0, v[10:11]
	global_load_dword v206, v[12:13], off
	global_load_dword v207, v[10:11], off
	v_cmp_eq_u32_e64 s[0:1], 0, v8
	v_add_u32_e32 v7, 0x800, v7
	s_or_b64 s[86:87], s[0:1], s[86:87]
	global_load_dword v208, v[12:13], off offset:16
	s_nop 0
	global_load_dword v209, v[10:11], off offset:16
	s_waitcnt vmcnt(6)
	ds_write2st64_b32 v9, v202, v203 offset1:8
	s_waitcnt vmcnt(4)
	ds_write2st64_b32 v9, v204, v205 offset0:36 offset1:44
	s_waitcnt vmcnt(2)
	ds_write2st64_b32 v9, v206, v207 offset0:16 offset1:24
	s_waitcnt vmcnt(0)
	ds_write2st64_b32 v9, v208, v209 offset0:52 offset1:60
	v_add_u32_e32 v9, 0x2000, v9
	v_mov_b32_e32 v10, s48
	s_andn2_b64 exec, exec, s[86:87]
	s_cbranch_execnz .LBB0_3640
	s_or_b64 exec, exec, s[86:87]
	v_lshlrev_b32_e32 v8, 9, v10

.LBB0_5003:
	v_and_b32_e32 v11, 0x7fffff80, v6
	v_and_b32_e32 v10, 0x7fffff80, v7
	v_add_u32_e32 v11, v11, v128
	v_add_u32_e32 v10, v10, v1
	v_sub_u32_e32 v12, 0x7ff, v11
	v_sub_u32_e32 v13, 0x7ff, v10
	v_cndmask_b32_e32 v11, v12, v11, vcc
	v_sub_u32_e32 v12, 0xff, v6
	v_cndmask_b32_e32 v10, v13, v10, vcc
	v_sub_u32_e32 v13, 0xff, v7
	v_cndmask_b32_e32 v12, v12, v6, vcc
	v_cmp_gt_i32_e64 s[2:3], s49, v6
	v_add_u32_e32 v11, s47, v11
	v_cndmask_b32_e32 v13, v13, v7, vcc
	v_add_u32_e32 v12, s30, v12
	v_cmp_gt_i32_e64 s[78:79], s49, v7
	v_add_u32_e32 v10, s47, v10
	v_add_u32_e32 v13, s30, v13
	v_cndmask_b32_e64 v12, v11, v12, s[2:3]
	v_cndmask_b32_e64 v10, v10, v13, s[78:79]
	v_ashrrev_i32_e32 v13, 31, v12
	v_ashrrev_i32_e32 v11, 31, v10
	v_lshlrev_b64 v[12:13], 6, v[12:13]
	v_lshlrev_b64 v[10:11], 6, v[10:11]
	v_lshl_add_u64 v[12:13], s[34:35], 0, v[12:13]
	v_lshl_add_u64 v[10:11], s[34:35], 0, v[10:11]
	global_load_dword v202, v[12:13], off
	global_load_dword v203, v[10:11], off
	v_add_u32_e32 v8, -2, v8
	s_add_i32 s36, s36, 4
	global_load_dword v204, v[12:13], off offset:16
	s_nop 0
	global_load_dword v205, v[10:11], off offset:16
	v_add_u32_e32 v11, 0x400, v6
	v_and_b32_e32 v13, 0x7fffff80, v11
	v_add_u32_e32 v13, v13, v128
	v_sub_u32_e32 v14, 0x7ff, v13
	v_cndmask_b32_e32 v13, v14, v13, vcc
	v_sub_u32_e32 v14, 0xfffffcff, v6
	v_cmp_gt_i32_e64 s[2:3], s49, v11
	v_cndmask_b32_e32 v11, v14, v11, vcc
	v_add_u32_e32 v13, s47, v13
	v_add_u32_e32 v11, s30, v11
	v_add_u32_e32 v6, 0x800, v6
	v_add_u32_e32 v10, 0x400, v7
	v_and_b32_e32 v12, 0x7fffff80, v10
	v_add_u32_e32 v12, v12, v1
	v_sub_u32_e32 v15, 0x7ff, v12
	v_cndmask_b32_e32 v12, v15, v12, vcc
	v_sub_u32_e32 v15, 0xfffffcff, v7
	v_cmp_gt_i32_e64 s[78:79], s49, v10
	v_cndmask_b32_e32 v10, v15, v10, vcc
	v_add_u32_e32 v12, s47, v12
	v_add_u32_e32 v10, s30, v10
	v_cndmask_b32_e64 v10, v12, v10, s[78:79]
	v_cndmask_b32_e64 v12, v13, v11, s[2:3]
	v_ashrrev_i32_e32 v13, 31, v12
	v_ashrrev_i32_e32 v11, 31, v10
	v_lshlrev_b64 v[12:13], 6, v[12:13]
	v_lshlrev_b64 v[10:11], 6, v[10:11]
	v_lshl_add_u64 v[12:13], s[34:35], 0, v[12:13]
	v_lshl_add_u64 v[10:11], s[34:35], 0, v[10:11]
	global_load_dword v206, v[12:13], off
	global_load_dword v207, v[10:11], off
	v_cmp_eq_u32_e64 s[2:3], 0, v8
	v_add_u32_e32 v7, 0x800, v7
	s_or_b64 s[86:87], s[2:3], s[86:87]
	global_load_dword v208, v[12:13], off offset:16
	s_nop 0
	global_load_dword v209, v[10:11], off offset:16
	s_waitcnt vmcnt(6)
	ds_write2st64_b32 v9, v202, v203 offset1:8
	s_waitcnt vmcnt(4)
	ds_write2st64_b32 v9, v204, v205 offset0:36 offset1:44
	s_waitcnt vmcnt(2)
	ds_write2st64_b32 v9, v206, v207 offset0:16 offset1:24
	s_waitcnt vmcnt(0)
	ds_write2st64_b32 v9, v208, v209 offset0:52 offset1:60
	v_add_u32_e32 v9, 0x2000, v9
	v_mov_b32_e32 v10, s36
	s_andn2_b64 exec, exec, s[86:87]
	s_cbranch_execnz .LBB0_5003
	s_or_b64 exec, exec, s[86:87]
	v_lshlrev_b32_e32 v8, 9, v10
